# v046 + LN1 row mean/variance wave sums (8 chains, 4 rows interleaved): ds_bpermute butterflies -> v_add_f32_dpp + row_bcast + v_readlane
# speedup vs baseline: 1.0033x; 1.0001x over previous
; __device__ __forceinline__ float bflo(unsigned w) { return __uint_as_float(w << 16); }
; __device__ __forceinline__ float bfhi(unsigned w) { return __uint_as_float(w & 0xffff0000u); }
; template <bool WB = true>
; __device__ __forceinline__ void ln1_phase(const bf16_t* buf, bf16_t* h1b, unsigned* xqs, float* sx, const float* gam, const float* bet, int G, int b) {
;     ...
;     for (int row0 = gw; row0 < S_; row0 += R * NGW) {
;         f32x4 v[R][8]; float sum[R], sq[R], amax[R];
; #pragma unroll
;         for (int q = 0; q < R; ++q) {
;             const int row = min(row0 + q * NGW, S_ - 1);
;             const bf16_t* rp = buf + (size_t)row * D_;
;             sum[q] = 0.f;
; #pragma unroll
;             for (int j = 0; j < 8; ++j) { const u32x2 w = *(const u32x2*)(rp + 256 * j + 4 * lane); v[q][j] = (f32x4){bflo(w.x), bfhi(w.x), bflo(w.y), bfhi(w.y)}; sum[q] += (v[q][j].x + v[q][j].y) + (v[q][j].z + v[q][j].w); }
;         }
.LBB0_543:
	v_mbcnt_lo_u32_b32 v219, -1, 0
	v_mbcnt_hi_u32_b32 v219, -1, v219
	s_add_u32 s30, s92, 0x17800000
	s_addc_u32 s31, s93, 0
	v_lshlrev_b32_e32 v219, 3, v219
	s_lshl_b32 s20, s4, 12
	s_add_u32 s20, s30, s20
	s_addc_u32 s21, s31, 0
	s_add_i32 s22, s62, s4
	s_min_i32 s22, s22, 0x3fff
	s_lshl_b32 s22, s22, 12
	s_add_u32 s22, s30, s22
	s_addc_u32 s23, s31, 0
	s_add_i32 s24, s5, s4
	s_min_i32 s24, s24, 0x3fff
	s_lshl_b32 s24, s24, 12
	s_add_u32 s24, s30, s24
	s_addc_u32 s25, s31, 0
	s_mul_i32 s26, s96, 24
	s_add_i32 s26, s26, s4
	s_min_i32 s26, s26, 0x3fff
	s_lshl_b32 s26, s26, 12
	s_add_u32 s26, s30, s26
	s_addc_u32 s27, s31, 0
	global_load_dwordx2 v[224:225], v219, s[20:21]
	global_load_dwordx2 v[226:227], v219, s[20:21] offset:512
	global_load_dwordx2 v[228:229], v219, s[20:21] offset:3584
	global_load_dwordx2 v[230:231], v219, s[20:21] offset:1536
	global_load_dwordx2 v[232:233], v219, s[20:21] offset:1024
	global_load_dwordx2 v[234:235], v219, s[20:21] offset:2048
	global_load_dwordx2 v[236:237], v219, s[20:21] offset:2560
	global_load_dwordx2 v[238:239], v219, s[20:21] offset:3072
	global_load_dwordx2 v[240:241], v219, s[22:23]
	global_load_dwordx2 v[244:245], v219, s[22:23] offset:512
	global_load_dwordx2 v[246:247], v219, s[22:23] offset:3584
	global_load_dwordx2 v[248:249], v219, s[22:23] offset:1536
	global_load_dwordx2 v[250:251], v219, s[22:23] offset:1024
	global_load_dwordx2 v[252:253], v219, s[22:23] offset:2048
	global_load_dwordx2 v[254:255], v219, s[22:23] offset:2560
	v_lshl_add_u64 v[44:45], s[92:93], 0, v[38:39]
	s_waitcnt vmcnt(14)
	v_mov_b64_e32 v[2:3], v[224:225]
	global_load_dwordx2 v[224:225], v219, s[22:23] offset:3072
	s_waitcnt vmcnt(14)
	v_mov_b64_e32 v[4:5], v[226:227]
	global_load_dwordx2 v[226:227], v219, s[24:25]
	s_add_i32 s56, s62, s4
	s_min_i32 s0, s56, 0x3fff
	s_ashr_i32 s1, s0, 31
	s_lshl_b64 s[0:1], s[0:1], 12
	s_add_i32 s58, s5, s4
	s_waitcnt vmcnt(14)
	v_mov_b64_e32 v[50:51], v[228:229]
	global_load_dwordx2 v[228:229], v219, s[24:25] offset:512
	v_lshlrev_b32_e32 v140, 16, v2
	v_lshlrev_b32_e32 v141, 16, v4
	v_and_b32_e32 v143, 0xffff0000, v4
	v_and_b32_e32 v142, 0xffff0000, v2
	v_lshlrev_b32_e32 v137, 16, v5
	v_lshlrev_b32_e32 v136, 16, v3
	v_and_b32_e32 v139, 0xffff0000, v5
	v_and_b32_e32 v138, 0xffff0000, v3
	v_pk_add_f32 v[2:3], v[140:141], v[142:143]
	v_pk_add_f32 v[4:5], v[136:137], v[138:139]
	v_lshlrev_b32_e32 v43, 16, v51
	v_pk_add_f32 v[2:3], v[2:3], v[4:5]
	s_waitcnt vmcnt(14)
	v_mov_b64_e32 v[4:5], v[230:231]
	global_load_dwordx2 v[230:231], v219, s[24:25] offset:3584
	v_add_f32_e32 v2, 0, v2
	v_add_f32_e32 v8, v2, v3
	s_waitcnt vmcnt(14)
	v_mov_b64_e32 v[2:3], v[232:233]
	global_load_dwordx2 v[232:233], v219, s[24:25] offset:1536
	v_and_b32_e32 v41, 0xffff0000, v51
	v_lshlrev_b32_e32 v64, 16, v4
	v_and_b32_e32 v65, 0xffff0000, v4
	v_lshlrev_b32_e32 v66, 16, v5
	v_and_b32_e32 v67, 0xffff0000, v5
	s_waitcnt vmcnt(14)
	v_mov_b64_e32 v[4:5], v[234:235]
	global_load_dwordx2 v[234:235], v219, s[24:25] offset:1024
	v_lshlrev_b32_e32 v77, 16, v3
	v_lshlrev_b32_e32 v76, 16, v2
	v_and_b32_e32 v145, 0xffff0000, v3
	v_and_b32_e32 v144, 0xffff0000, v2
	v_pk_add_f32 v[2:3], v[76:77], v[144:145]
	v_add_f32_e32 v58, v64, v65
	v_pk_add_f32 v[2:3], v[2:3], v[2:3] op_sel:[0,1] op_sel_hi:[1,0]
	v_add_f32_e32 v56, v66, v67
	v_and_b32_e32 v61, 0xffff0000, v4
	s_waitcnt lgkmcnt(0)
	v_lshlrev_b32_e32 v9, 16, v4
	v_lshlrev_b32_e32 v59, 16, v5
	v_and_b32_e32 v57, 0xffff0000, v5
	v_mov_b32_e32 v3, v61
	v_pk_add_f32 v[2:3], v[8:9], v[2:3]
	v_pk_add_f32 v[4:5], v[58:59], v[56:57]
	s_nop 0
	v_pk_add_f32 v[46:47], v[2:3], v[4:5]
	s_waitcnt vmcnt(14)
	v_mov_b64_e32 v[2:3], v[236:237]
	global_load_dwordx2 v[236:237], v219, s[24:25] offset:2048
	s_waitcnt vmcnt(14)
	v_mov_b64_e32 v[4:5], v[238:239]
	global_load_dwordx2 v[238:239], v219, s[24:25] offset:2560
	v_lshlrev_b32_e32 v44, 16, v50
	v_and_b32_e32 v45, 0xffff0000, v50
	v_pk_add_f32 v[46:47], v[46:47], v[46:47] op_sel:[0,1] op_sel_hi:[1,0]
	v_lshl_add_u64 v[50:51], v[12:13], 0, s[0:1]
	v_mov_b32_e32 v47, v44
	s_min_i32 s0, s58, 0x3fff
	s_ashr_i32 s1, s0, 31
	s_lshl_b64 s[0:1], s[0:1], 12
	v_lshlrev_b32_e32 v7, 16, v3
	v_lshlrev_b32_e32 v6, 16, v2
	v_and_b32_e32 v147, 0xffff0000, v3
	v_and_b32_e32 v146, 0xffff0000, v2
	v_pk_add_f32 v[48:49], v[6:7], v[146:147]
	v_lshlrev_b32_e32 v2, 16, v4
	v_and_b32_e32 v3, 0xffff0000, v4
	v_lshlrev_b32_e32 v4, 16, v5
	v_and_b32_e32 v5, 0xffff0000, v5
	v_pk_add_f32 v[48:49], v[48:49], v[48:49] op_sel:[0,1] op_sel_hi:[1,0]
	v_add_f32_e32 v42, v2, v3
	v_add_f32_e32 v40, v4, v5
	v_mov_b32_e32 v49, v45
	v_pk_add_f32 v[46:47], v[46:47], v[48:49]
	v_pk_add_f32 v[48:49], v[42:43], v[40:41]
	s_nop 0
	v_pk_add_f32 v[46:47], v[46:47], v[48:49]
	s_nop 0
	v_add_f32_e32 v8, v46, v47
	s_waitcnt vmcnt(14)
	v_mov_b64_e32 v[46:47], v[240:241]
	global_load_dwordx2 v[240:241], v219, s[24:25] offset:3072
	s_waitcnt vmcnt(14)
	v_mov_b64_e32 v[48:49], v[244:245]
	global_load_dwordx2 v[244:245], v219, s[26:27]
	s_waitcnt vmcnt(14)
	v_mov_b64_e32 v[82:83], v[246:247]
	global_load_dwordx2 v[246:247], v219, s[26:27] offset:512
	v_lshlrev_b32_e32 v156, 16, v46
	v_lshlrev_b32_e32 v157, 16, v48
	v_and_b32_e32 v159, 0xffff0000, v48
	v_and_b32_e32 v158, 0xffff0000, v46
	v_lshlrev_b32_e32 v153, 16, v49
	v_lshlrev_b32_e32 v152, 16, v47
	v_and_b32_e32 v155, 0xffff0000, v49
	v_and_b32_e32 v154, 0xffff0000, v47
	v_pk_add_f32 v[46:47], v[156:157], v[158:159]
	v_pk_add_f32 v[48:49], v[152:153], v[154:155]
	s_nop 0
	v_pk_add_f32 v[46:47], v[46:47], v[48:49]
	s_waitcnt vmcnt(14)
; __device__ __forceinline__ float bflo(unsigned w) { return __uint_as_float(w << 16); }
; __device__ __forceinline__ float bfhi(unsigned w) { return __uint_as_float(w & 0xffff0000u); }
; __device__ __forceinline__ float wave_sum(float v) {
; #pragma unroll
;     for (int o = 1; o < 64; o <<= 1) v += __shfl_xor(v, o);
;     return v;
; template <bool WB = true>
; __device__ __forceinline__ void ln1_phase(const bf16_t* buf, bf16_t* h1b, unsigned* xqs, float* sx, const float* gam, const float* bet, int G, int b) {
;     ...
;             for (int j = 0; j < 8; ++j) { const u32x2 w = *(const u32x2*)(rp + 256 * j + 4 * lane); v[q][j] = (f32x4){bflo(w.x), bfhi(w.x), bflo(w.y), bfhi(w.y)}; sum[q] += (v[q][j].x + v[q][j].y) + (v[q][j].z + v[q][j].w); }
;         }
; #pragma unroll
;         for (int q = 0; q < R; ++q) sum[q] = wave_sum(sum[q]) * (1.0f / D_);
; #pragma unroll
;         for (int q = 0; q < R; ++q) { sq[q] = 0.f;
; #pragma unroll
;             for (int j = 0; j < 8; ++j) { v[q][j] = v[q][j] - sum[q]; sq[q] += (v[q][j].x * v[q][j].x + v[q][j].y * v[q][j].y) + (v[q][j].z * v[q][j].z + v[q][j].w * v[q][j].w); } }
	v_mov_b64_e32 v[48:49], v[248:249]
	global_load_dwordx2 v[248:249], v219, s[26:27] offset:3584
	v_add_f32_e32 v10, 0, v46
	v_add_f32_e32 v68, v10, v47
	s_waitcnt vmcnt(14)
	v_mov_b64_e32 v[46:47], v[250:251]
	global_load_dwordx2 v[250:251], v219, s[26:27] offset:1536
	v_lshlrev_b32_e32 v84, 16, v48
	v_and_b32_e32 v85, 0xffff0000, v48
	v_lshlrev_b32_e32 v86, 16, v49
	v_and_b32_e32 v87, 0xffff0000, v49
	s_waitcnt vmcnt(14)
	v_mov_b64_e32 v[48:49], v[252:253]
	global_load_dwordx2 v[252:253], v219, s[26:27] offset:1024
	v_lshlrev_b32_e32 v89, 16, v47
	v_lshlrev_b32_e32 v88, 16, v46
	v_and_b32_e32 v151, 0xffff0000, v47
	v_and_b32_e32 v150, 0xffff0000, v46
	v_pk_add_f32 v[46:47], v[88:89], v[150:151]
	v_add_f32_e32 v72, v84, v85
	v_pk_add_f32 v[46:47], v[46:47], v[46:47] op_sel:[0,1] op_sel_hi:[1,0]
	v_add_f32_e32 v70, v86, v87
	v_and_b32_e32 v75, 0xffff0000, v48
	v_lshlrev_b32_e32 v69, 16, v48
	v_lshlrev_b32_e32 v73, 16, v49
	v_and_b32_e32 v71, 0xffff0000, v49
	v_mov_b32_e32 v47, v75
	v_pk_add_f32 v[46:47], v[68:69], v[46:47]
	v_pk_add_f32 v[48:49], v[72:73], v[70:71]
	s_nop 0
	v_pk_add_f32 v[78:79], v[46:47], v[48:49]
	s_waitcnt vmcnt(14)
	v_mov_b64_e32 v[46:47], v[254:255]
	global_load_dwordx2 v[254:255], v219, s[26:27] offset:2048
	v_pk_add_f32 v[78:79], v[78:79], v[78:79] op_sel:[0,1] op_sel_hi:[1,0]
	v_lshlrev_b32_e32 v49, 16, v83
	v_lshlrev_b32_e32 v63, 16, v47
	v_lshlrev_b32_e32 v62, 16, v46
	v_and_b32_e32 v149, 0xffff0000, v47
	v_and_b32_e32 v148, 0xffff0000, v46
	s_waitcnt vmcnt(14)
	v_mov_b64_e32 v[46:47], v[224:225]
	global_load_dwordx2 v[224:225], v219, s[26:27] offset:2560
	v_pk_add_f32 v[80:81], v[62:63], v[148:149]
	v_lshlrev_b32_e32 v50, 16, v82
	v_and_b32_e32 v51, 0xffff0000, v82
	v_pk_add_f32 v[80:81], v[80:81], v[80:81] op_sel:[0,1] op_sel_hi:[1,0]
	v_mov_b32_e32 v79, v50
	v_mov_b32_e32 v81, v51
	v_pk_add_f32 v[78:79], v[78:79], v[80:81]
	v_lshlrev_b32_e32 v52, 16, v46
	v_and_b32_e32 v53, 0xffff0000, v46
	v_lshlrev_b32_e32 v54, 16, v47
	v_and_b32_e32 v55, 0xffff0000, v47
	v_add_f32_e32 v48, v52, v53
	v_add_f32_e32 v46, v54, v55
	v_and_b32_e32 v47, 0xffff0000, v83
	v_pk_add_f32 v[80:81], v[48:49], v[46:47]
	v_lshl_add_u64 v[82:83], v[12:13], 0, s[0:1]
	v_pk_add_f32 v[78:79], v[78:79], v[80:81]
	s_mul_i32 s0, s96, 24
	v_add_f32_e32 v10, v78, v79
	s_waitcnt vmcnt(14)
	v_mov_b64_e32 v[78:79], v[226:227]
	global_load_dwordx2 v[226:227], v219, s[26:27] offset:3072
	s_waitcnt vmcnt(14)
	v_mov_b64_e32 v[80:81], v[228:229]
	s_add_i32 s60, s0, s4
	s_min_i32 s0, s60, 0x3fff
	s_ashr_i32 s1, s0, 31
	s_lshl_b64 s[0:1], s[0:1], 12
	s_nop 1
	s_waitcnt vmcnt(13)
	v_mov_b64_e32 v[100:101], v[230:231]
	s_waitcnt lgkmcnt(0)
	v_add_f32_dpp v8, v8, v8 quad_perm:[1,0,3,2] row_mask:0xf bank_mask:0xf
	s_nop 1
	s_waitcnt lgkmcnt(0)
	v_add_f32_dpp v8, v8, v8 quad_perm:[2,3,0,1] row_mask:0xf bank_mask:0xf
	s_nop 1
	s_waitcnt lgkmcnt(0)
	v_add_f32_dpp v8, v8, v8 row_half_mirror row_mask:0xf bank_mask:0xf
	s_nop 1
	s_waitcnt lgkmcnt(0)
	v_add_f32_dpp v8, v8, v8 row_mirror row_mask:0xf bank_mask:0xf
	s_nop 1
	s_waitcnt lgkmcnt(0)
	v_add_f32_dpp v8, v8, v8 row_bcast:15 row_mask:0xa bank_mask:0xf
	s_nop 1
	s_waitcnt lgkmcnt(0)
	v_add_f32_dpp v56, v8, v8 row_bcast:31 row_mask:0xc bank_mask:0xf
	s_nop 1
	v_readlane_b32 s98, v56, 63
	s_nop 1
	v_mov_b32_e32 v56, s98
	s_nop 1
	v_fmac_f32_e32 v142, 0xba000000, v56
	v_fmac_f32_e32 v143, 0xba000000, v56
	v_fmac_f32_e32 v138, 0xba000000, v56
	v_fmac_f32_e32 v140, 0xba000000, v56
	s_waitcnt lgkmcnt(0)
	v_add_f32_dpp v8, v10, v10 quad_perm:[1,0,3,2] row_mask:0xf bank_mask:0xf
	s_nop 1
	v_fmac_f32_e32 v139, 0xba000000, v56
	v_fmac_f32_e32 v141, 0xba000000, v56
	v_mov_b32_e32 v185, v142
	v_fmac_f32_e32 v136, 0xba000000, v56
	s_waitcnt lgkmcnt(0)
	v_add_f32_dpp v8, v8, v8 quad_perm:[2,3,0,1] row_mask:0xf bank_mask:0xf
	s_nop 1
	v_fmac_f32_e32 v137, 0xba000000, v56
	v_mov_b32_e32 v184, v140
	v_fmac_f32_e32 v144, 0xba000000, v56
	v_fmac_f32_e32 v145, 0xba000000, v56
	s_waitcnt lgkmcnt(0)
	v_add_f32_dpp v8, v8, v8 row_half_mirror row_mask:0xf bank_mask:0xf
	s_nop 1
	v_fmac_f32_e32 v77, 0xba000000, v56
	v_fmac_f32_e32 v76, 0xba000000, v56
	v_fmac_f32_e32 v64, 0xba000000, v56
	v_fmac_f32_e32 v65, 0xba000000, v56
	s_waitcnt lgkmcnt(0)
	v_add_f32_dpp v8, v8, v8 row_mirror row_mask:0xf bank_mask:0xf
	s_nop 1
	v_fmac_f32_e32 v66, 0xba000000, v56
	v_fmac_f32_e32 v67, 0xba000000, v56
	v_fmac_f32_e32 v57, 0xba000000, v56
	v_fmac_f32_e32 v59, 0xba000000, v56
	s_waitcnt lgkmcnt(0)
	v_add_f32_dpp v8, v8, v8 row_bcast:15 row_mask:0xa bank_mask:0xf
	s_nop 1
	v_fmac_f32_e32 v61, 0xba000000, v56
	v_fmac_f32_e32 v9, 0xba000000, v56
	v_fmac_f32_e32 v146, 0xba000000, v56
	v_fmac_f32_e32 v147, 0xba000000, v56
	s_waitcnt lgkmcnt(0)
	v_add_f32_dpp v48, v8, v8 row_bcast:31 row_mask:0xc bank_mask:0xf
	s_nop 1
	v_readlane_b32 s98, v48, 63
	s_nop 1
	v_mov_b32_e32 v48, s98
	v_fmac_f32_e32 v7, 0xba000000, v56
	v_fmac_f32_e32 v6, 0xba000000, v56
	v_lshlrev_b32_e32 v164, 16, v78
	v_lshlrev_b32_e32 v165, 16, v80
	v_and_b32_e32 v171, 0xffff0000, v80
	v_and_b32_e32 v170, 0xffff0000, v78
	v_lshlrev_b32_e32 v161, 16, v81
	v_lshlrev_b32_e32 v160, 16, v79
	v_and_b32_e32 v163, 0xffff0000, v81
	v_and_b32_e32 v162, 0xffff0000, v79
	v_pk_add_f32 v[78:79], v[164:165], v[170:171]
	v_pk_add_f32 v[80:81], v[160:161], v[162:163]
	v_fmac_f32_e32 v2, 0xba000000, v56
	v_pk_add_f32 v[78:79], v[78:79], v[80:81]
	s_waitcnt vmcnt(12)
	v_mov_b64_e32 v[80:81], v[232:233]
	v_add_f32_e32 v40, 0, v78
	v_add_f32_e32 v90, v40, v79
	s_waitcnt vmcnt(11)
; __device__ __forceinline__ float bflo(unsigned w) { return __uint_as_float(w << 16); }
; __device__ __forceinline__ float bfhi(unsigned w) { return __uint_as_float(w & 0xffff0000u); }
; template <bool WB = true>
; __device__ __forceinline__ void ln1_phase(const bf16_t* buf, bf16_t* h1b, unsigned* xqs, float* sx, const float* gam, const float* bet, int G, int b) {
;     ...
;             for (int j = 0; j < 8; ++j) { const u32x2 w = *(const u32x2*)(rp + 256 * j + 4 * lane); v[q][j] = (f32x4){bflo(w.x), bfhi(w.x), bflo(w.y), bfhi(w.y)}; sum[q] += (v[q][j].x + v[q][j].y) + (v[q][j].z + v[q][j].w); }
;         }
; #pragma unroll
;         for (int q = 0; q < R; ++q) sum[q] = wave_sum(sum[q]) * (1.0f / D_);
; #pragma unroll
;         for (int q = 0; q < R; ++q) { sq[q] = 0.f;
; #pragma unroll
;             for (int j = 0; j < 8; ++j) { v[q][j] = v[q][j] - sum[q]; sq[q] += (v[q][j].x * v[q][j].x + v[q][j].y * v[q][j].y) + (v[q][j].z * v[q][j].z + v[q][j].w * v[q][j].w); } }
	v_mov_b64_e32 v[78:79], v[234:235]
	v_fmac_f32_e32 v3, 0xba000000, v56
	v_fmac_f32_e32 v4, 0xba000000, v56
	v_fmac_f32_e32 v5, 0xba000000, v56
	v_fmac_f32_e32 v41, 0xba000000, v56
	v_fmac_f32_e32 v43, 0xba000000, v56
	v_fmac_f32_e32 v45, 0xba000000, v56
	v_fmac_f32_e32 v44, 0xba000000, v56
	v_fmac_f32_e32 v154, 0xba000000, v48
	v_fmac_f32_e32 v152, 0xba000000, v48
	v_fmac_f32_e32 v158, 0xba000000, v48
	v_fmac_f32_e32 v156, 0xba000000, v48
	v_fmac_f32_e32 v155, 0xba000000, v48
	v_fmac_f32_e32 v153, 0xba000000, v48
	v_fmac_f32_e32 v159, 0xba000000, v48
	v_fmac_f32_e32 v157, 0xba000000, v48
	v_fmac_f32_e32 v150, 0xba000000, v48
	v_fmac_f32_e32 v88, 0xba000000, v48
	v_fmac_f32_e32 v151, 0xba000000, v48
	v_fmac_f32_e32 v89, 0xba000000, v48
	v_fmac_f32_e32 v85, 0xba000000, v48
	v_fmac_f32_e32 v84, 0xba000000, v48
	v_fmac_f32_e32 v87, 0xba000000, v48
	v_fmac_f32_e32 v86, 0xba000000, v48
	v_fmac_f32_e32 v71, 0xba000000, v48
	v_fmac_f32_e32 v73, 0xba000000, v48
	v_fmac_f32_e32 v75, 0xba000000, v48
	v_fmac_f32_e32 v69, 0xba000000, v48
	v_fmac_f32_e32 v148, 0xba000000, v48
	v_fmac_f32_e32 v62, 0xba000000, v48
	v_fmac_f32_e32 v149, 0xba000000, v48
	v_fmac_f32_e32 v63, 0xba000000, v48
	v_fmac_f32_e32 v53, 0xba000000, v48
	v_fmac_f32_e32 v52, 0xba000000, v48
	v_fmac_f32_e32 v55, 0xba000000, v48
	v_fmac_f32_e32 v54, 0xba000000, v48
	v_fmac_f32_e32 v47, 0xba000000, v48
	v_fmac_f32_e32 v49, 0xba000000, v48
	v_fmac_f32_e32 v51, 0xba000000, v48
	v_fmac_f32_e32 v50, 0xba000000, v48
	v_mov_b32_e32 v186, v89
	v_mov_b32_e32 v187, v151
	v_mov_b32_e32 v89, v150
	v_pk_mul_f32 v[150:151], v[88:89], v[88:89]
	v_mov_b32_e32 v74, v69
	v_mov_b32_e32 v70, v73
	v_lshlrev_b32_e32 v112, 16, v80
	v_and_b32_e32 v113, 0xffff0000, v80
	v_lshlrev_b32_e32 v114, 16, v81
	v_and_b32_e32 v115, 0xffff0000, v81
	s_waitcnt vmcnt(10)
	v_mov_b64_e32 v[80:81], v[236:237]
	v_lshlrev_b32_e32 v105, 16, v79
	v_lshlrev_b32_e32 v104, 16, v78
	v_and_b32_e32 v173, 0xffff0000, v79
	v_and_b32_e32 v172, 0xffff0000, v78
	v_pk_add_f32 v[78:79], v[104:105], v[172:173]
	v_add_f32_e32 v108, v112, v113
	v_pk_add_f32 v[78:79], v[78:79], v[78:79] op_sel:[0,1] op_sel_hi:[1,0]
	v_add_f32_e32 v106, v114, v115
	v_and_b32_e32 v111, 0xffff0000, v80
	v_lshlrev_b32_e32 v91, 16, v80
	v_lshlrev_b32_e32 v109, 16, v81
	v_and_b32_e32 v107, 0xffff0000, v81
	v_mov_b32_e32 v79, v111
	v_pk_add_f32 v[78:79], v[90:91], v[78:79]
	v_pk_add_f32 v[80:81], v[108:109], v[106:107]
	s_nop 0
	v_pk_add_f32 v[96:97], v[78:79], v[80:81]
	s_waitcnt vmcnt(9)
	v_mov_b64_e32 v[78:79], v[238:239]
	v_pk_add_f32 v[96:97], v[96:97], v[96:97] op_sel:[0,1] op_sel_hi:[1,0]
	v_lshlrev_b32_e32 v81, 16, v101
	v_lshlrev_b32_e32 v103, 16, v79
	v_lshlrev_b32_e32 v102, 16, v78
	v_and_b32_e32 v175, 0xffff0000, v79
	v_and_b32_e32 v174, 0xffff0000, v78
	s_waitcnt vmcnt(8)
	v_mov_b64_e32 v[78:79], v[240:241]
	v_pk_add_f32 v[98:99], v[102:103], v[174:175]
	v_lshlrev_b32_e32 v82, 16, v100
	v_and_b32_e32 v83, 0xffff0000, v100
	v_pk_add_f32 v[98:99], v[98:99], v[98:99] op_sel:[0,1] op_sel_hi:[1,0]
	v_mov_b32_e32 v97, v82
	v_mov_b32_e32 v99, v83
	v_pk_add_f32 v[96:97], v[96:97], v[98:99]
	v_lshlrev_b32_e32 v92, 16, v78
	v_and_b32_e32 v93, 0xffff0000, v78
	v_lshlrev_b32_e32 v94, 16, v79
	v_and_b32_e32 v95, 0xffff0000, v79
	v_add_f32_e32 v80, v92, v93
	v_add_f32_e32 v78, v94, v95
	v_and_b32_e32 v79, 0xffff0000, v101
	v_pk_add_f32 v[98:99], v[80:81], v[78:79]
	v_lshl_add_u64 v[100:101], v[12:13], 0, s[0:1]
	v_pk_add_f32 v[96:97], v[96:97], v[98:99]
	s_nop 0
	v_add_f32_e32 v40, v96, v97
	s_waitcnt vmcnt(7)
	v_mov_b64_e32 v[96:97], v[244:245]
	s_waitcnt vmcnt(6)
	v_mov_b64_e32 v[98:99], v[246:247]
	s_waitcnt vmcnt(5)
	v_mov_b64_e32 v[182:183], v[248:249]
	s_nop 1
	s_waitcnt lgkmcnt(0)
	v_add_f32_dpp v8, v40, v40 quad_perm:[1,0,3,2] row_mask:0xf bank_mask:0xf
	s_nop 1
	s_waitcnt lgkmcnt(0)
	v_add_f32_dpp v8, v8, v8 quad_perm:[2,3,0,1] row_mask:0xf bank_mask:0xf
	s_nop 1
	s_waitcnt lgkmcnt(0)
	v_add_f32_dpp v8, v8, v8 row_half_mirror row_mask:0xf bank_mask:0xf
	s_nop 1
	s_waitcnt lgkmcnt(0)
	v_add_f32_dpp v8, v8, v8 row_mirror row_mask:0xf bank_mask:0xf
	s_nop 1
	s_waitcnt lgkmcnt(0)
	v_add_f32_dpp v8, v8, v8 row_bcast:15 row_mask:0xa bank_mask:0xf
	s_nop 1
	s_waitcnt lgkmcnt(0)
	v_add_f32_dpp v8, v8, v8 row_bcast:31 row_mask:0xc bank_mask:0xf
	s_nop 1
	v_readlane_b32 s98, v8, 63
	s_nop 1
	v_mov_b32_e32 v8, s98
	v_fmac_f32_e32 v162, 0xba000000, v8
	v_fmac_f32_e32 v170, 0xba000000, v8
	v_fmac_f32_e32 v163, 0xba000000, v8
	v_fmac_f32_e32 v171, 0xba000000, v8
	v_fmac_f32_e32 v160, 0xba000000, v8
	v_fmac_f32_e32 v164, 0xba000000, v8
	v_fmac_f32_e32 v161, 0xba000000, v8
	v_fmac_f32_e32 v165, 0xba000000, v8
	v_fmac_f32_e32 v172, 0xba000000, v8
	v_fmac_f32_e32 v173, 0xba000000, v8
	v_fmac_f32_e32 v105, 0xba000000, v8
	v_fmac_f32_e32 v104, 0xba000000, v8
	v_fmac_f32_e32 v112, 0xba000000, v8
	v_fmac_f32_e32 v113, 0xba000000, v8
	v_fmac_f32_e32 v114, 0xba000000, v8
	v_fmac_f32_e32 v115, 0xba000000, v8
	v_fmac_f32_e32 v107, 0xba000000, v8
	v_fmac_f32_e32 v109, 0xba000000, v8
	v_fmac_f32_e32 v111, 0xba000000, v8
	v_fmac_f32_e32 v91, 0xba000000, v8
	v_fmac_f32_e32 v174, 0xba000000, v8
	v_fmac_f32_e32 v175, 0xba000000, v8
	v_fmac_f32_e32 v103, 0xba000000, v8
	v_fmac_f32_e32 v102, 0xba000000, v8
	v_fmac_f32_e32 v92, 0xba000000, v8
	v_fmac_f32_e32 v93, 0xba000000, v8
	v_fmac_f32_e32 v94, 0xba000000, v8
	v_fmac_f32_e32 v95, 0xba000000, v8
	v_fmac_f32_e32 v79, 0xba000000, v8
	v_fmac_f32_e32 v81, 0xba000000, v8
	v_fmac_f32_e32 v83, 0xba000000, v8
	v_fmac_f32_e32 v82, 0xba000000, v8
	v_mov_b32_e32 v110, v91
	v_mov_b32_e32 v106, v109
	v_mov_b32_e32 v78, v81
	v_lshlrev_b32_e32 v190, 16, v96
	v_lshlrev_b32_e32 v191, 16, v98
	v_and_b32_e32 v193, 0xffff0000, v98
	v_and_b32_e32 v192, 0xffff0000, v96
	v_lshlrev_b32_e32 v179, 16, v99
	v_lshlrev_b32_e32 v178, 16, v97
	v_and_b32_e32 v189, 0xffff0000, v99
	v_and_b32_e32 v188, 0xffff0000, v97
	v_pk_add_f32 v[96:97], v[190:191], v[192:193]
	v_pk_add_f32 v[98:99], v[178:179], v[188:189]
	s_nop 0
	v_pk_add_f32 v[96:97], v[96:97], v[98:99]
	s_waitcnt vmcnt(4)
; __device__ __forceinline__ float bflo(unsigned w) { return __uint_as_float(w << 16); }
; __device__ __forceinline__ float bfhi(unsigned w) { return __uint_as_float(w & 0xffff0000u); }
; template <bool WB = true>
; __device__ __forceinline__ void ln1_phase(const bf16_t* buf, bf16_t* h1b, unsigned* xqs, float* sx, const float* gam, const float* bet, int G, int b) {
;     ...
;             for (int j = 0; j < 8; ++j) { const u32x2 w = *(const u32x2*)(rp + 256 * j + 4 * lane); v[q][j] = (f32x4){bflo(w.x), bfhi(w.x), bflo(w.y), bfhi(w.y)}; sum[q] += (v[q][j].x + v[q][j].y) + (v[q][j].z + v[q][j].w); }
;         }
; #pragma unroll
;         for (int q = 0; q < R; ++q) sum[q] = wave_sum(sum[q]) * (1.0f / D_);
; #pragma unroll
;         for (int q = 0; q < R; ++q) { sq[q] = 0.f;
; #pragma unroll
;             for (int j = 0; j < 8; ++j) { v[q][j] = v[q][j] - sum[q]; sq[q] += (v[q][j].x * v[q][j].x + v[q][j].y * v[q][j].y) + (v[q][j].z * v[q][j].z + v[q][j].w * v[q][j].w); } }
; #pragma unroll
;         for (int q = 0; q < R; ++q) sq[q] = 1.0f / sqrtf(wave_sum(sq[q]) * (1.0f / D_) + LN_EPS);
; #pragma unroll
;         for (int j = 0; j < 8; ++j) {
;             const f32x4 gg = *(const f32x4*)(gam + 256 * j + 4 * lane), bb = *(const f32x4*)(bet + 256 * j + 4 * lane);
	v_mov_b64_e32 v[98:99], v[250:251]
	v_add_f32_e32 v42, 0, v96
	v_add_f32_e32 v120, v42, v97
	s_waitcnt vmcnt(3)
	v_mov_b64_e32 v[96:97], v[252:253]
	v_lshlrev_b32_e32 v130, 16, v98
	v_and_b32_e32 v131, 0xffff0000, v98
	v_lshlrev_b32_e32 v132, 16, v99
	v_and_b32_e32 v133, 0xffff0000, v99
	s_waitcnt vmcnt(2)
	v_mov_b64_e32 v[98:99], v[254:255]
	v_lshlrev_b32_e32 v135, 16, v97
	v_lshlrev_b32_e32 v134, 16, v96
	v_and_b32_e32 v195, 0xffff0000, v97
	v_and_b32_e32 v194, 0xffff0000, v96
	v_pk_add_f32 v[96:97], v[134:135], v[194:195]
	v_add_f32_e32 v126, v130, v131
	v_pk_add_f32 v[96:97], v[96:97], v[96:97] op_sel:[0,1] op_sel_hi:[1,0]
	v_add_f32_e32 v124, v132, v133
	v_and_b32_e32 v129, 0xffff0000, v98
	v_lshlrev_b32_e32 v121, 16, v98
	v_lshlrev_b32_e32 v127, 16, v99
	v_and_b32_e32 v125, 0xffff0000, v99
	v_mov_b32_e32 v97, v129
	v_pk_add_f32 v[96:97], v[120:121], v[96:97]
	v_pk_add_f32 v[98:99], v[126:127], v[124:125]
	s_nop 0
	v_pk_add_f32 v[176:177], v[96:97], v[98:99]
	s_waitcnt vmcnt(1)
	v_mov_b64_e32 v[96:97], v[224:225]
	v_pk_add_f32 v[176:177], v[176:177], v[176:177] op_sel:[0,1] op_sel_hi:[1,0]
	v_lshlrev_b32_e32 v99, 16, v183
	v_lshlrev_b32_e32 v123, 16, v97
	v_lshlrev_b32_e32 v122, 16, v96
	v_and_b32_e32 v197, 0xffff0000, v97
	v_and_b32_e32 v196, 0xffff0000, v96
	s_waitcnt vmcnt(0)
	v_mov_b64_e32 v[96:97], v[226:227]
	global_load_dwordx4 v[224:227], v[14:15], off
	global_load_dwordx4 v[228:231], v[16:17], off
	global_load_dwordx4 v[232:235], v[14:15], off offset:1024
	global_load_dwordx4 v[236:239], v[16:17], off offset:1024
	global_load_dwordx4 v[244:247], v[14:15], off offset:2048
	global_load_dwordx4 v[248:251], v[16:17], off offset:2048
	global_load_dwordx4 v[252:255], v[14:15], off offset:3072
	v_pk_add_f32 v[180:181], v[122:123], v[196:197]
	v_lshlrev_b32_e32 v100, 16, v182
	v_and_b32_e32 v101, 0xffff0000, v182
	v_pk_add_f32 v[180:181], v[180:181], v[180:181] op_sel:[0,1] op_sel_hi:[1,0]
	v_mov_b32_e32 v177, v100
	v_mov_b32_e32 v181, v101
	v_pk_add_f32 v[176:177], v[176:177], v[180:181]
	v_mov_b32_e32 v182, v137
	v_lshlrev_b32_e32 v116, 16, v96
	v_and_b32_e32 v117, 0xffff0000, v96
	v_lshlrev_b32_e32 v118, 16, v97
	v_and_b32_e32 v119, 0xffff0000, v97
	v_add_f32_e32 v98, v116, v117
	v_add_f32_e32 v96, v118, v119
	v_and_b32_e32 v97, 0xffff0000, v183
	v_pk_add_f32 v[180:181], v[98:99], v[96:97]
	v_mov_b32_e32 v183, v139
	v_pk_add_f32 v[176:177], v[176:177], v[180:181]
	v_mov_b32_e32 v181, v143
	v_add_f32_e32 v42, v176, v177
	s_nop 1
	v_pk_mul_f32 v[142:143], v[142:143], v[142:143]
	v_mov_b32_e32 v180, v141
	v_pk_fma_f32 v[140:141], v[140:141], v[140:141], v[142:143]
	v_mov_b32_e32 v143, v138
	s_waitcnt lgkmcnt(0)
	v_add_f32_dpp v10, v42, v42 quad_perm:[1,0,3,2] row_mask:0xf bank_mask:0xf
	s_nop 1
	v_pk_mul_f32 v[138:139], v[138:139], v[138:139]
	v_mov_b32_e32 v142, v136
	v_pk_fma_f32 v[136:137], v[136:137], v[136:137], v[138:139]
	v_mov_b32_e32 v176, v77
	s_waitcnt lgkmcnt(0)
	v_add_f32_dpp v10, v10, v10 quad_perm:[2,3,0,1] row_mask:0xf bank_mask:0xf
	s_nop 1
	v_mov_b32_e32 v177, v145
	v_mov_b32_e32 v77, v144
	v_pk_add_f32 v[136:137], v[140:141], v[136:137]
	v_pk_mul_f32 v[138:139], v[176:177], v[176:177]
	s_waitcnt lgkmcnt(0)
	v_add_f32_dpp v10, v10, v10 row_half_mirror row_mask:0xf bank_mask:0xf
	s_nop 1
	v_pk_mul_f32 v[140:141], v[76:77], v[76:77]
	v_pk_add_f32 v[136:137], v[136:137], v[136:137] op_sel_hi:[0,1]
	v_pk_mov_b32 v[144:145], v[140:141], v[138:139] op_sel:[1,0]
	v_mov_b32_e32 v141, v139
	s_waitcnt lgkmcnt(0)
	v_add_f32_dpp v10, v10, v10 row_mirror row_mask:0xf bank_mask:0xf
	s_nop 1
	v_pk_add_f32 v[138:139], v[144:145], v[140:141]
	v_mul_f32_e32 v136, v57, v57
	v_pk_add_f32 v[138:139], v[138:139], v[138:139] op_sel_hi:[0,1]
	v_mul_f32_e32 v138, v59, v59
	s_waitcnt lgkmcnt(0)
	v_add_f32_dpp v10, v10, v10 row_bcast:15 row_mask:0xa bank_mask:0xf
	s_nop 1
	v_pk_add_f32 v[136:137], v[138:139], v[136:137]
	s_waitcnt lgkmcnt(0)
	v_add_f32_dpp v46, v10, v10 row_bcast:31 row_mask:0xc bank_mask:0xf
	s_nop 1
	v_readlane_b32 s98, v46, 63
	s_nop 1
	v_mov_b32_e32 v46, s98
	v_mul_f32_e32 v10, v64, v64
	v_pk_fma_f32 v[140:141], v[64:65], v[64:65], v[10:11] op_sel_hi:[1,1,0]
	v_mul_f32_e32 v10, v66, v66
	v_pk_fma_f32 v[144:145], v[66:67], v[66:67], v[10:11] op_sel_hi:[1,1,0]
	v_mul_f32_e32 v140, v9, v9
	v_mul_f32_e32 v144, v61, v61
	v_pk_add_f32 v[140:141], v[140:141], v[144:145]
	v_mul_f32_e32 v10, v2, v2
	v_pk_add_f32 v[136:137], v[140:141], v[136:137]
	v_mov_b32_e32 v140, v7
	v_mov_b32_e32 v141, v147
	v_mov_b32_e32 v7, v146
	v_pk_mul_f32 v[138:139], v[140:141], v[140:141]
	v_pk_mul_f32 v[144:145], v[6:7], v[6:7]
	v_pk_add_f32 v[136:137], v[136:137], v[136:137] op_sel_hi:[0,1]
	v_pk_mov_b32 v[146:147], v[144:145], v[138:139] op_sel:[1,0]
	v_mov_b32_e32 v145, v139
	v_pk_add_f32 v[138:139], v[146:147], v[144:145]
	v_pk_fma_f32 v[144:145], v[2:3], v[2:3], v[10:11] op_sel_hi:[1,1,0]
	v_mul_f32_e32 v10, v4, v4
	v_pk_add_f32 v[138:139], v[138:139], v[138:139] op_sel_hi:[0,1]
	v_pk_fma_f32 v[146:147], v[4:5], v[4:5], v[10:11] op_sel_hi:[1,1,0]
	v_mul_f32_e32 v144, v44, v44
	v_mul_f32_e32 v146, v45, v45
	v_mul_f32_e32 v138, v43, v43
	v_mul_f32_e32 v136, v41, v41
	v_pk_add_f32 v[144:145], v[144:145], v[146:147]
	v_pk_add_f32 v[136:137], v[138:139], v[136:137]
	v_fmac_f32_e32 v188, 0xba000000, v46
	v_pk_add_f32 v[136:137], v[144:145], v[136:137]
	v_fmac_f32_e32 v178, 0xba000000, v46
	v_add_f32_e32 v10, v136, v137
	v_fmac_f32_e32 v192, 0xba000000, v46
	v_fmac_f32_e32 v190, 0xba000000, v46
	v_fmac_f32_e32 v189, 0xba000000, v46
	v_fmac_f32_e32 v179, 0xba000000, v46
	v_fmac_f32_e32 v193, 0xba000000, v46
	v_fmac_f32_e32 v191, 0xba000000, v46
	v_fmac_f32_e32 v194, 0xba000000, v46
	v_fmac_f32_e32 v134, 0xba000000, v46
	v_fmac_f32_e32 v195, 0xba000000, v46
	v_fmac_f32_e32 v135, 0xba000000, v46
	v_fmac_f32_e32 v131, 0xba000000, v46
	v_fmac_f32_e32 v130, 0xba000000, v46
	v_fmac_f32_e32 v133, 0xba000000, v46
	v_fmac_f32_e32 v132, 0xba000000, v46
	v_fmac_f32_e32 v125, 0xba000000, v46
	v_fmac_f32_e32 v127, 0xba000000, v46
	v_fmac_f32_e32 v129, 0xba000000, v46
	v_fmac_f32_e32 v121, 0xba000000, v46
	v_fmac_f32_e32 v196, 0xba000000, v46
	v_fmac_f32_e32 v122, 0xba000000, v46
	v_fmac_f32_e32 v197, 0xba000000, v46
	v_fmac_f32_e32 v123, 0xba000000, v46
	v_fmac_f32_e32 v117, 0xba000000, v46
	v_fmac_f32_e32 v116, 0xba000000, v46
	v_fmac_f32_e32 v119, 0xba000000, v46
	v_fmac_f32_e32 v118, 0xba000000, v46
	v_fmac_f32_e32 v97, 0xba000000, v46
	v_fmac_f32_e32 v99, 0xba000000, v46
	v_fmac_f32_e32 v101, 0xba000000, v46
	v_fmac_f32_e32 v100, 0xba000000, v46
	s_nop 1
	v_pk_mul_f32 v[138:139], v[158:159], v[158:159]
	v_mov_b32_e32 v146, v157
	v_pk_fma_f32 v[144:145], v[156:157], v[156:157], v[138:139]
	v_mov_b32_e32 v157, v155
	s_waitcnt lgkmcnt(0)
; template <bool WB = true>
; __device__ __forceinline__ void ln1_phase(const bf16_t* buf, bf16_t* h1b, unsigned* xqs, float* sx, const float* gam, const float* bet, int G, int b) {
;     ...
;         for (int q = 0; q < R; ++q) { sq[q] = 0.f;
; #pragma unroll
;             for (int j = 0; j < 8; ++j) { v[q][j] = v[q][j] - sum[q]; sq[q] += (v[q][j].x * v[q][j].x + v[q][j].y * v[q][j].y) + (v[q][j].z * v[q][j].z + v[q][j].w * v[q][j].w); } }
; #pragma unroll
;         for (int q = 0; q < R; ++q) sq[q] = 1.0f / sqrtf(wave_sum(sq[q]) * (1.0f / D_) + LN_EPS);
	v_add_f32_dpp v10, v10, v10 quad_perm:[1,0,3,2] row_mask:0xf bank_mask:0xf
	s_nop 1
	v_mov_b32_e32 v139, v154
	v_pk_mul_f32 v[154:155], v[154:155], v[154:155]
	v_mov_b32_e32 v136, v156
	v_mov_b32_e32 v156, v153
	s_waitcnt lgkmcnt(0)
	v_add_f32_dpp v10, v10, v10 quad_perm:[2,3,0,1] row_mask:0xf bank_mask:0xf
	s_nop 1
	v_mov_b32_e32 v138, v152
	v_pk_fma_f32 v[152:153], v[152:153], v[152:153], v[154:155]
	v_mul_f32_e32 v40, v84, v84
	v_pk_add_f32 v[144:145], v[144:145], v[152:153]
	s_waitcnt lgkmcnt(0)
	v_add_f32_dpp v10, v10, v10 row_half_mirror row_mask:0xf bank_mask:0xf
	s_nop 1
	v_pk_mul_f32 v[152:153], v[186:187], v[186:187]
	v_pk_add_f32 v[144:145], v[144:145], v[144:145] op_sel_hi:[0,1]
	v_pk_mov_b32 v[154:155], v[150:151], v[152:153] op_sel:[1,0]
	v_mov_b32_e32 v151, v153
	s_waitcnt lgkmcnt(0)
	v_add_f32_dpp v10, v10, v10 row_mirror row_mask:0xf bank_mask:0xf
	s_nop 1
	v_pk_add_f32 v[150:151], v[154:155], v[150:151]
	v_pk_fma_f32 v[152:153], v[84:85], v[84:85], v[40:41] op_sel_hi:[1,1,0]
	v_mul_f32_e32 v40, v86, v86
	v_pk_add_f32 v[150:151], v[150:151], v[150:151] op_sel_hi:[0,1]
	s_waitcnt lgkmcnt(0)
	v_add_f32_dpp v10, v10, v10 row_bcast:15 row_mask:0xa bank_mask:0xf
	s_nop 1
	v_pk_fma_f32 v[154:155], v[86:87], v[86:87], v[40:41] op_sel_hi:[1,1,0]
	v_mul_f32_e32 v152, v69, v69
	v_mul_f32_e32 v154, v75, v75
	v_mul_f32_e32 v150, v73, v73
	s_waitcnt lgkmcnt(0)
	v_add_f32_dpp v10, v10, v10 row_bcast:31 row_mask:0xc bank_mask:0xf
	s_nop 1
	v_readlane_b32 s98, v10, 63
	s_nop 1
	v_mov_b32_e32 v10, s98
	v_fmamk_f32 v10, v10, 0x3a000000, v217
	v_cmp_gt_f32_e32 vcc, s45, v10
	v_mul_f32_e32 v46, 0x4f800000, v10
	v_mul_f32_e32 v144, v71, v71
	v_cndmask_b32_e32 v10, v10, v46, vcc
	v_sqrt_f32_e32 v46, v10
	v_pk_add_f32 v[152:153], v[152:153], v[154:155]
	v_pk_add_f32 v[144:145], v[150:151], v[144:145]
	v_mov_b32_e32 v150, v63
	v_add_u32_e32 v48, -1, v46
	v_fma_f32 v56, -v48, v46, v10
	v_cmp_ge_f32_e64 s[0:1], 0, v56
	v_add_u32_e32 v56, 1, v46
	v_mov_b32_e32 v151, v149
	v_cndmask_b32_e64 v48, v46, v48, s[0:1]
	v_fma_f32 v46, -v56, v46, v10
	v_cmp_lt_f32_e64 s[0:1], 0, v46
	v_mov_b32_e32 v63, v148
	v_pk_add_f32 v[144:145], v[152:153], v[144:145]
	v_cndmask_b32_e64 v46, v48, v56, s[0:1]
	v_mul_f32_e32 v48, 0x37800000, v46
	v_cndmask_b32_e32 v46, v46, v48, vcc
	v_cmp_class_f32_e32 vcc, v10, v218
	v_pk_mul_f32 v[152:153], v[150:151], v[150:151]
	v_pk_mul_f32 v[148:149], v[62:63], v[62:63]
	v_cndmask_b32_e32 v10, v46, v10, vcc
	v_div_scale_f32 v46, s[0:1], v10, v10, 1.0
	v_rcp_f32_e32 v48, v46
	v_pk_mov_b32 v[154:155], v[148:149], v[152:153] op_sel:[1,0]
	v_mov_b32_e32 v149, v153
	v_mul_f32_e32 v40, v52, v52
	v_fma_f32 v56, -v46, v48, 1.0
	v_pk_add_f32 v[148:149], v[154:155], v[148:149]
	v_pk_fma_f32 v[152:153], v[52:53], v[52:53], v[40:41] op_sel_hi:[1,1,0]
	v_mul_f32_e32 v40, v54, v54
	v_fmac_f32_e32 v48, v56, v48
	v_div_scale_f32 v56, vcc, 1.0, v10, 1.0
	v_pk_add_f32 v[144:145], v[144:145], v[144:145] op_sel_hi:[0,1]
	v_pk_add_f32 v[148:149], v[148:149], v[148:149] op_sel_hi:[0,1]
	v_pk_fma_f32 v[154:155], v[54:55], v[54:55], v[40:41] op_sel_hi:[1,1,0]
	v_mul_f32_e32 v58, v56, v48
	v_mul_f32_e32 v152, v50, v50
	v_mul_f32_e32 v154, v51, v51
	v_mul_f32_e32 v148, v49, v49
	v_mul_f32_e32 v144, v47, v47
	v_fma_f32 v60, -v46, v58, v56
	v_pk_add_f32 v[152:153], v[152:153], v[154:155]
	v_pk_add_f32 v[144:145], v[148:149], v[144:145]
	v_fmac_f32_e32 v58, v60, v48
	v_pk_add_f32 v[144:145], v[152:153], v[144:145]
	v_fma_f32 v46, -v46, v58, v56
	v_add_f32_e32 v42, v144, v145
	v_div_fmas_f32 v46, v46, v48, v58
	v_div_fixup_f32 v10, v46, v10, 1.0
	s_nop 1
	v_pk_mul_f32 v[152:153], v[170:171], v[170:171]
	v_pk_mul_f32 v[154:155], v[162:163], v[162:163]
	v_mov_b32_e32 v147, v159
	v_mov_b32_e32 v148, v165
	s_waitcnt lgkmcnt(0)
	v_add_f32_dpp v42, v42, v42 quad_perm:[1,0,3,2] row_mask:0xf bank_mask:0xf
	s_nop 1
	v_pk_fma_f32 v[152:153], v[164:165], v[164:165], v[152:153]
	v_mov_b32_e32 v159, v163
	v_mov_b32_e32 v165, v162
	v_pk_fma_f32 v[154:155], v[160:161], v[160:161], v[154:155]
	s_waitcnt lgkmcnt(0)
	v_add_f32_dpp v42, v42, v42 quad_perm:[2,3,0,1] row_mask:0xf bank_mask:0xf
	s_nop 1
	v_mov_b32_e32 v162, v105
	v_mov_b32_e32 v163, v173
	v_mov_b32_e32 v105, v172
	v_mov_b32_e32 v137, v158
	s_waitcnt lgkmcnt(0)
	v_add_f32_dpp v42, v42, v42 row_half_mirror row_mask:0xf bank_mask:0xf
	s_nop 1
	v_mov_b32_e32 v144, v164
	v_mov_b32_e32 v158, v161
	v_mov_b32_e32 v164, v160
	v_pk_add_f32 v[152:153], v[152:153], v[154:155]
	s_waitcnt lgkmcnt(0)
	v_add_f32_dpp v42, v42, v42 row_mirror row_mask:0xf bank_mask:0xf
	s_nop 1
	v_pk_mul_f32 v[154:155], v[162:163], v[162:163]
	v_pk_mul_f32 v[160:161], v[104:105], v[104:105]
	v_mov_b32_e32 v149, v171
	v_mov_b32_e32 v145, v170
	s_waitcnt lgkmcnt(0)
	v_add_f32_dpp v42, v42, v42 row_bcast:15 row_mask:0xa bank_mask:0xf
	s_nop 1
	v_pk_mov_b32 v[170:171], v[160:161], v[154:155] op_sel:[1,0]
	v_mov_b32_e32 v161, v155
	v_mul_f32_e32 v40, v112, v112
	v_pk_add_f32 v[154:155], v[170:171], v[160:161]
	s_waitcnt lgkmcnt(0)
; template <bool WB = true>
; __device__ __forceinline__ void ln1_phase(const bf16_t* buf, bf16_t* h1b, unsigned* xqs, float* sx, const float* gam, const float* bet, int G, int b) {
;     ...
;         for (int q = 0; q < R; ++q) { sq[q] = 0.f;
; #pragma unroll
;             for (int j = 0; j < 8; ++j) { v[q][j] = v[q][j] - sum[q]; sq[q] += (v[q][j].x * v[q][j].x + v[q][j].y * v[q][j].y) + (v[q][j].z * v[q][j].z + v[q][j].w * v[q][j].w); } }
; #pragma unroll
;         for (int q = 0; q < R; ++q) sq[q] = 1.0f / sqrtf(wave_sum(sq[q]) * (1.0f / D_) + LN_EPS);
; #pragma unroll
;         for (int j = 0; j < 8; ++j) {
;             const f32x4 gg = *(const f32x4*)(gam + 256 * j + 4 * lane), bb = *(const f32x4*)(bet + 256 * j + 4 * lane);
	v_add_f32_dpp v42, v42, v42 row_bcast:31 row_mask:0xc bank_mask:0xf
	s_nop 1
	v_readlane_b32 s98, v42, 63
	s_nop 1
	v_mov_b32_e32 v42, s98
	v_fmamk_f32 v42, v42, 0x3a000000, v217
	v_cmp_gt_f32_e32 vcc, s45, v42
	v_mul_f32_e32 v46, 0x4f800000, v42
	v_pk_fma_f32 v[160:161], v[112:113], v[112:113], v[40:41] op_sel_hi:[1,1,0]
	v_cndmask_b32_e32 v42, v42, v46, vcc
	v_sqrt_f32_e32 v46, v42
	v_mul_f32_e32 v40, v114, v114
	v_pk_add_f32 v[152:153], v[152:153], v[152:153] op_sel_hi:[0,1]
	v_pk_add_f32 v[154:155], v[154:155], v[154:155] op_sel_hi:[0,1]
	v_add_u32_e32 v48, -1, v46
	v_fma_f32 v56, -v48, v46, v42
	v_cmp_ge_f32_e64 s[0:1], 0, v56
	v_add_u32_e32 v56, 1, v46
	v_pk_fma_f32 v[170:171], v[114:115], v[114:115], v[40:41] op_sel_hi:[1,1,0]
	v_cndmask_b32_e64 v48, v46, v48, s[0:1]
	v_fma_f32 v46, -v56, v46, v42
	v_cmp_lt_f32_e64 s[0:1], 0, v46
	v_mul_f32_e32 v160, v91, v91
	v_mul_f32_e32 v170, v111, v111
	v_cndmask_b32_e64 v46, v48, v56, s[0:1]
	v_mul_f32_e32 v48, 0x37800000, v46
	v_cndmask_b32_e32 v46, v46, v48, vcc
	v_cmp_class_f32_e32 vcc, v42, v218
	v_mul_f32_e32 v154, v109, v109
	v_mul_f32_e32 v152, v107, v107
	v_cndmask_b32_e32 v42, v46, v42, vcc
	v_div_scale_f32 v46, s[0:1], v42, v42, 1.0
	v_rcp_f32_e32 v48, v46
	v_pk_add_f32 v[160:161], v[160:161], v[170:171]
	v_pk_add_f32 v[152:153], v[154:155], v[152:153]
	v_mul_f32_e32 v40, v92, v92
	v_pk_add_f32 v[152:153], v[160:161], v[152:153]
	v_mov_b32_e32 v160, v103
	v_mov_b32_e32 v161, v175
	v_mov_b32_e32 v103, v174
	v_pk_mul_f32 v[154:155], v[160:161], v[160:161]
	v_pk_mul_f32 v[170:171], v[102:103], v[102:103]
	v_fma_f32 v56, -v46, v48, 1.0
	v_pk_mov_b32 v[172:173], v[170:171], v[154:155] op_sel:[1,0]
	v_mov_b32_e32 v171, v155
	v_pk_add_f32 v[154:155], v[172:173], v[170:171]
	v_pk_fma_f32 v[170:171], v[92:93], v[92:93], v[40:41] op_sel_hi:[1,1,0]
	v_mul_f32_e32 v40, v94, v94
	v_fmac_f32_e32 v48, v56, v48
	v_div_scale_f32 v56, vcc, 1.0, v42, 1.0
	v_pk_add_f32 v[152:153], v[152:153], v[152:153] op_sel_hi:[0,1]
	v_pk_add_f32 v[154:155], v[154:155], v[154:155] op_sel_hi:[0,1]
	v_pk_fma_f32 v[172:173], v[94:95], v[94:95], v[40:41] op_sel_hi:[1,1,0]
	v_mul_f32_e32 v58, v56, v48
	v_mul_f32_e32 v170, v82, v82
	v_mul_f32_e32 v172, v83, v83
	v_mul_f32_e32 v154, v81, v81
	v_mul_f32_e32 v152, v79, v79
	v_fma_f32 v60, -v46, v58, v56
	v_pk_add_f32 v[170:171], v[170:171], v[172:173]
	v_pk_add_f32 v[152:153], v[154:155], v[152:153]
	v_fmac_f32_e32 v58, v60, v48
	v_pk_add_f32 v[152:153], v[170:171], v[152:153]
	v_fma_f32 v46, -v46, v58, v56
	v_add_f32_e32 v40, v152, v153
	v_div_fmas_f32 v46, v46, v48, v58
	v_div_fixup_f32 v42, v46, v42, 1.0
	s_nop 1
	v_pk_mul_f32 v[152:153], v[192:193], v[192:193]
	v_pk_mul_f32 v[154:155], v[188:189], v[188:189]
	v_mov_b32_e32 v199, v193
	v_mov_b32_e32 v170, v190
	s_waitcnt lgkmcnt(0)
	v_add_f32_dpp v40, v40, v40 quad_perm:[1,0,3,2] row_mask:0xf bank_mask:0xf
	s_nop 1
	v_mov_b32_e32 v171, v192
	v_pk_fma_f32 v[152:153], v[190:191], v[190:191], v[152:153]
	v_mov_b32_e32 v190, v179
	v_mov_b32_e32 v200, v178
	s_waitcnt lgkmcnt(0)
	v_add_f32_dpp v40, v40, v40 quad_perm:[2,3,0,1] row_mask:0xf bank_mask:0xf
	s_nop 1
	v_pk_fma_f32 v[154:155], v[178:179], v[178:179], v[154:155]
	v_mov_b32_e32 v192, v135
	v_mov_b32_e32 v193, v195
	v_mov_b32_e32 v135, v194
	s_waitcnt lgkmcnt(0)
	v_add_f32_dpp v40, v40, v40 row_half_mirror row_mask:0xf bank_mask:0xf
	s_nop 1
	v_mov_b32_e32 v178, v123
	v_mov_b32_e32 v179, v197
	v_mov_b32_e32 v123, v196
	s_waitcnt vmcnt(6)
	v_mov_b64_e32 v[194:195], v[224:225]
	v_mov_b64_e32 v[196:197], v[226:227]
	global_load_dwordx4 v[224:227], v[16:17], off offset:3072
	s_waitcnt vmcnt(6)
	v_mov_b64_e32 v[220:221], v[228:229]
	v_mov_b64_e32 v[222:223], v[230:231]
	global_load_dwordx4 v[228:231], v[20:21], off
	s_waitcnt lgkmcnt(0)
	v_add_f32_dpp v40, v40, v40 row_mirror row_mask:0xf bank_mask:0xf
	s_nop 1
	v_pk_add_f32 v[152:153], v[152:153], v[154:155]
	v_pk_mul_f32 v[154:155], v[192:193], v[192:193]
	v_pk_mul_f32 v[172:173], v[134:135], v[134:135]
	v_mul_f32_e32 v8, v130, v130
	s_waitcnt lgkmcnt(0)
	v_add_f32_dpp v40, v40, v40 row_bcast:15 row_mask:0xa bank_mask:0xf
	s_nop 1
	v_pk_mov_b32 v[174:175], v[172:173], v[154:155] op_sel:[1,0]
	v_mov_b32_e32 v173, v155
	v_pk_add_f32 v[154:155], v[174:175], v[172:173]
	v_pk_fma_f32 v[172:173], v[130:131], v[130:131], v[8:9] op_sel_hi:[1,1,0]
	s_waitcnt lgkmcnt(0)
; template <bool WB = true>
; __device__ __forceinline__ void ln1_phase(const bf16_t* buf, bf16_t* h1b, unsigned* xqs, float* sx, const float* gam, const float* bet, int G, int b) {
;     ...
;         for (int q = 0; q < R; ++q) { sq[q] = 0.f;
; #pragma unroll
;             for (int j = 0; j < 8; ++j) { v[q][j] = v[q][j] - sum[q]; sq[q] += (v[q][j].x * v[q][j].x + v[q][j].y * v[q][j].y) + (v[q][j].z * v[q][j].z + v[q][j].w * v[q][j].w); } }
; #pragma unroll
;         for (int q = 0; q < R; ++q) sq[q] = 1.0f / sqrtf(wave_sum(sq[q]) * (1.0f / D_) + LN_EPS);
; #pragma unroll
;         for (int j = 0; j < 8; ++j) {
;             const f32x4 gg = *(const f32x4*)(gam + 256 * j + 4 * lane), bb = *(const f32x4*)(bet + 256 * j + 4 * lane);
; #pragma unroll
;             for (int q = 0; q < R; ++q) v[q][j] = v[q][j] * sq[q] * gg + bb;
	v_add_f32_dpp v40, v40, v40 row_bcast:31 row_mask:0xc bank_mask:0xf
	s_nop 1
	v_readlane_b32 s98, v40, 63
	s_nop 1
	v_mov_b32_e32 v40, s98
	v_fmamk_f32 v40, v40, 0x3a000000, v217
	v_cmp_gt_f32_e32 vcc, s45, v40
	v_mul_f32_e32 v46, 0x4f800000, v40
	v_mul_f32_e32 v8, v132, v132
	v_cndmask_b32_e32 v40, v40, v46, vcc
	v_sqrt_f32_e32 v46, v40
	v_pk_add_f32 v[152:153], v[152:153], v[152:153] op_sel_hi:[0,1]
	v_pk_add_f32 v[154:155], v[154:155], v[154:155] op_sel_hi:[0,1]
	v_pk_fma_f32 v[174:175], v[132:133], v[132:133], v[8:9] op_sel_hi:[1,1,0]
	v_add_u32_e32 v48, -1, v46
	v_fma_f32 v56, -v48, v46, v40
	v_cmp_ge_f32_e64 s[0:1], 0, v56
	v_add_u32_e32 v56, 1, v46
	v_mul_f32_e32 v172, v121, v121
	v_cndmask_b32_e64 v48, v46, v48, s[0:1]
	v_fma_f32 v46, -v56, v46, v40
	v_cmp_lt_f32_e64 s[0:1], 0, v46
	v_mul_f32_e32 v174, v129, v129
	v_mul_f32_e32 v154, v127, v127
	v_cndmask_b32_e64 v46, v48, v56, s[0:1]
	v_mul_f32_e32 v48, 0x37800000, v46
	v_cndmask_b32_e32 v46, v46, v48, vcc
	v_cmp_class_f32_e32 vcc, v40, v218
	v_mul_f32_e32 v152, v125, v125
	v_pk_add_f32 v[172:173], v[172:173], v[174:175]
	v_cndmask_b32_e32 v40, v46, v40, vcc
	v_div_scale_f32 v46, s[0:1], v40, v40, 1.0
	v_rcp_f32_e32 v48, v46
	v_pk_add_f32 v[152:153], v[154:155], v[152:153]
	v_pk_mul_f32 v[154:155], v[178:179], v[178:179]
	v_pk_add_f32 v[152:153], v[172:173], v[152:153]
	v_pk_mul_f32 v[172:173], v[122:123], v[122:123]
	v_mul_f32_e32 v8, v116, v116
	v_pk_mov_b32 v[174:175], v[172:173], v[154:155] op_sel:[1,0]
	v_mov_b32_e32 v173, v155
	v_fma_f32 v56, -v46, v48, 1.0
	v_pk_add_f32 v[154:155], v[174:175], v[172:173]
	v_pk_fma_f32 v[172:173], v[116:117], v[116:117], v[8:9] op_sel_hi:[1,1,0]
	v_mul_f32_e32 v8, v118, v118
	v_fmac_f32_e32 v48, v56, v48
	v_div_scale_f32 v56, vcc, 1.0, v40, 1.0
	v_pk_add_f32 v[152:153], v[152:153], v[152:153] op_sel_hi:[0,1]
	v_pk_add_f32 v[154:155], v[154:155], v[154:155] op_sel_hi:[0,1]
	v_pk_fma_f32 v[174:175], v[118:119], v[118:119], v[8:9] op_sel_hi:[1,1,0]
	v_mul_f32_e32 v58, v56, v48
	v_mul_f32_e32 v172, v100, v100
	v_mul_f32_e32 v174, v101, v101
	v_mul_f32_e32 v154, v99, v99
	v_mul_f32_e32 v152, v97, v97
	v_fma_f32 v60, -v46, v58, v56
	v_pk_add_f32 v[172:173], v[172:173], v[174:175]
	v_pk_add_f32 v[152:153], v[154:155], v[152:153]
	v_fmac_f32_e32 v58, v60, v48
	v_pk_add_f32 v[152:153], v[172:173], v[152:153]
	v_fma_f32 v46, -v46, v58, v56
	v_add_f32_e32 v8, v152, v153
	v_div_fmas_f32 v46, v46, v48, v58
	v_div_fixup_f32 v48, v46, v40, 1.0
	s_nop 1
	v_pk_mul_f32 v[152:153], v[184:185], v[10:11] op_sel_hi:[1,0]
	v_pk_mul_f32 v[136:137], v[136:137], v[42:43] op_sel_hi:[1,0]
	v_pk_mul_f32 v[138:139], v[138:139], v[42:43] op_sel_hi:[1,0]
	v_mov_b32_e32 v201, v188
	s_waitcnt lgkmcnt(0)
	v_add_f32_dpp v8, v8, v8 quad_perm:[1,0,3,2] row_mask:0xf bank_mask:0xf
	s_nop 1
	v_pk_mul_f32 v[142:143], v[142:143], v[10:11] op_sel_hi:[1,0]
	v_pk_fma_f32 v[174:175], v[152:153], v[194:195], v[220:221]
	v_pk_fma_f32 v[152:153], v[138:139], v[196:197], v[222:223]
	v_pk_fma_f32 v[154:155], v[136:137], v[194:195], v[220:221]
	s_waitcnt lgkmcnt(0)
	v_add_f32_dpp v8, v8, v8 quad_perm:[2,3,0,1] row_mask:0xf bank_mask:0xf
	s_nop 1
	v_pk_mul_f32 v[136:137], v[144:145], v[48:49] op_sel_hi:[1,0]
	v_pk_mul_f32 v[138:139], v[164:165], v[48:49] op_sel_hi:[1,0]
	v_pk_fma_f32 v[172:173], v[142:143], v[196:197], v[222:223]
	v_pk_fma_f32 v[142:143], v[196:197], v[138:139], v[222:223]
	s_waitcnt lgkmcnt(0)
	v_add_f32_dpp v8, v8, v8 row_half_mirror row_mask:0xf bank_mask:0xf
	s_nop 1
	v_pk_fma_f32 v[144:145], v[194:195], v[136:137], v[220:221]
	v_pk_mul_f32 v[146:147], v[146:147], v[42:43] op_sel_hi:[1,0]
	v_mov_b32_e32 v198, v191
	v_mov_b32_e32 v191, v189
	s_waitcnt lgkmcnt(0)
	v_add_f32_dpp v8, v8, v8 row_mirror row_mask:0xf bank_mask:0xf
	s_nop 1
	v_pk_mul_f32 v[164:165], v[180:181], v[10:11] op_sel_hi:[1,0]
	v_pk_mul_f32 v[156:157], v[156:157], v[42:43] op_sel_hi:[1,0]
	v_pk_mul_f32 v[76:77], v[76:77], v[10:11] op_sel_hi:[1,0]
	v_pk_mul_f32 v[176:177], v[176:177], v[10:11] op_sel_hi:[1,0]
	s_waitcnt lgkmcnt(0)
	v_add_f32_dpp v8, v8, v8 row_bcast:15 row_mask:0xa bank_mask:0xf
	s_nop 1
	v_pk_mul_f32 v[64:65], v[64:65], v[10:11] op_sel_hi:[1,0]
	v_pk_mul_f32 v[66:67], v[66:67], v[10:11] op_sel_hi:[1,0]
	v_mov_b32_e32 v128, v121
	v_mov_b32_e32 v124, v127
	s_waitcnt lgkmcnt(0)
	v_add_f32_dpp v8, v8, v8 row_bcast:31 row_mask:0xc bank_mask:0xf
	s_nop 1
	v_readlane_b32 s98, v8, 63
	s_nop 1
	v_mov_b32_e32 v8, s98
	v_fmamk_f32 v8, v8, 0x3a000000, v217
	v_cmp_gt_f32_e32 vcc, s45, v8
	v_mul_f32_e32 v40, 0x4f800000, v8
	v_pk_mul_f32 v[6:7], v[6:7], v[10:11] op_sel_hi:[1,0]
	v_cndmask_b32_e32 v8, v8, v40, vcc
	v_sqrt_f32_e32 v40, v8
	v_pk_mul_f32 v[2:3], v[2:3], v[10:11] op_sel_hi:[1,0]
	v_pk_mul_f32 v[4:5], v[4:5], v[10:11] op_sel_hi:[1,0]
	v_pk_mul_f32 v[44:45], v[44:45], v[10:11] op_sel_hi:[1,0]
	v_add_u32_e32 v46, -1, v40
	v_fma_f32 v56, -v46, v40, v8
	v_cmp_ge_f32_e64 s[0:1], 0, v56
	v_add_u32_e32 v56, 1, v40
	v_mov_b32_e32 v96, v99
	v_cndmask_b32_e64 v46, v40, v46, s[0:1]
	v_fma_f32 v40, -v56, v40, v8
	v_cmp_lt_f32_e64 s[0:1], 0, v40
	s_nop 1
	v_cndmask_b32_e64 v40, v46, v56, s[0:1]
	v_mul_f32_e32 v46, 0x37800000, v40
	v_cndmask_b32_e32 v40, v40, v46, vcc
	v_cmp_class_f32_e32 vcc, v8, v218
	s_nop 1
	v_cndmask_b32_e32 v8, v40, v8, vcc
	v_div_scale_f32 v40, s[0:1], v8, v8, 1.0
	v_rcp_f32_e32 v46, v40
	s_nop 0
	v_fma_f32 v56, -v40, v46, 1.0
	v_fmac_f32_e32 v46, v56, v46
	v_div_scale_f32 v56, vcc, 1.0, v8, 1.0
	v_mul_f32_e32 v58, v56, v46
	v_fma_f32 v60, -v40, v58, v56
	v_fmac_f32_e32 v58, v60, v46
	v_fma_f32 v40, -v40, v58, v56
	v_div_fmas_f32 v40, v40, v46, v58
	v_div_fixup_f32 v72, v40, v8, 1.0
	v_pk_mul_f32 v[138:139], v[170:171], v[72:73] op_sel_hi:[1,0]
	v_pk_mul_f32 v[136:137], v[200:201], v[72:73] op_sel_hi:[1,0]
	v_pk_fma_f32 v[138:139], v[194:195], v[138:139], v[220:221]
	v_pk_fma_f32 v[136:137], v[196:197], v[136:137], v[222:223]
	s_waitcnt vmcnt(6)
; template <bool WB = true>
; __device__ __forceinline__ void ln1_phase(const bf16_t* buf, bf16_t* h1b, unsigned* xqs, float* sx, const float* gam, const float* bet, int G, int b) {
;     ...
; #pragma unroll
;         for (int j = 0; j < 8; ++j) {
;             const f32x4 gg = *(const f32x4*)(gam + 256 * j + 4 * lane), bb = *(const f32x4*)(bet + 256 * j + 4 * lane);
; #pragma unroll
;             for (int q = 0; q < R; ++q) v[q][j] = v[q][j] * sq[q] * gg + bb;
;         }
; #pragma unroll
;         for (int q = 0; q < R; ++q) { amax[q] = 0.f;
; #pragma unroll
;             for (int j = 0; j < 8; ++j) amax[q] = fmaxf(amax[q], fmaxf(fmaxf(fabsf(v[q][j].x), fabsf(v[q][j].y)), fmaxf(fabsf(v[q][j].z), fabsf(v[q][j].w)))); }
	v_mov_b64_e32 v[194:195], v[232:233]
	v_mov_b64_e32 v[196:197], v[234:235]
	global_load_dwordx4 v[232:235], v[22:23], off
	s_waitcnt vmcnt(6)
	v_mov_b64_e32 v[220:221], v[236:237]
	v_mov_b64_e32 v[222:223], v[238:239]
	global_load_dwordx4 v[236:239], v[24:25], off
	v_pk_mul_f32 v[170:171], v[182:183], v[10:11] op_sel_hi:[1,0]
	v_mov_b32_e32 v60, v9
	v_mov_b32_e32 v56, v59
	v_pk_mul_f32 v[8:9], v[60:61], v[10:11] op_sel_hi:[1,0]
	v_pk_mul_f32 v[56:57], v[56:57], v[10:11] op_sel_hi:[1,0]
	v_mov_b32_e32 v40, v43
	v_pk_mul_f32 v[40:41], v[40:41], v[10:11] op_sel_hi:[1,0]
	v_mov_b32_e32 v46, v49
	v_pk_fma_f32 v[182:183], v[170:171], v[196:197], v[222:223]
	v_pk_fma_f32 v[170:171], v[146:147], v[194:195], v[220:221]
	v_pk_mul_f32 v[146:147], v[148:149], v[48:49] op_sel_hi:[1,0]
	v_pk_mul_f32 v[148:149], v[158:159], v[48:49] op_sel_hi:[1,0]
	v_pk_fma_f32 v[184:185], v[164:165], v[194:195], v[220:221]
	v_pk_fma_f32 v[164:165], v[156:157], v[196:197], v[222:223]
	v_pk_fma_f32 v[156:157], v[196:197], v[148:149], v[222:223]
	v_pk_fma_f32 v[158:159], v[194:195], v[146:147], v[220:221]
	v_pk_mul_f32 v[148:149], v[198:199], v[72:73] op_sel_hi:[1,0]
	v_pk_mul_f32 v[146:147], v[190:191], v[72:73] op_sel_hi:[1,0]
	v_pk_fma_f32 v[148:149], v[194:195], v[148:149], v[220:221]
	v_pk_fma_f32 v[146:147], v[196:197], v[146:147], v[222:223]
	s_waitcnt vmcnt(6)
	v_mov_b64_e32 v[194:195], v[244:245]
	v_mov_b64_e32 v[196:197], v[246:247]
	global_load_dwordx4 v[244:247], v[26:27], off
	s_waitcnt vmcnt(6)
	v_mov_b64_e32 v[198:199], v[248:249]
	v_mov_b64_e32 v[200:201], v[250:251]
	global_load_dwordx4 v[248:251], v[28:29], off
	v_pk_fma_f32 v[190:191], v[76:77], v[194:195], v[198:199]
	v_pk_mul_f32 v[76:77], v[88:89], v[42:43] op_sel_hi:[1,0]
	v_pk_mul_f32 v[88:89], v[186:187], v[42:43] op_sel_hi:[1,0]
	v_pk_fma_f32 v[188:189], v[176:177], v[196:197], v[200:201]
	v_pk_fma_f32 v[176:177], v[88:89], v[196:197], v[200:201]
	v_pk_fma_f32 v[180:181], v[76:77], v[194:195], v[198:199]
	v_pk_mul_f32 v[76:77], v[104:105], v[48:49] op_sel_hi:[1,0]
	v_pk_mul_f32 v[88:89], v[162:163], v[48:49] op_sel_hi:[1,0]
	v_pk_fma_f32 v[162:163], v[76:77], v[194:195], v[198:199]
	v_pk_fma_f32 v[104:105], v[88:89], v[196:197], v[200:201]
	v_pk_mul_f32 v[88:89], v[134:135], v[72:73] op_sel_hi:[1,0]
	v_pk_mul_f32 v[76:77], v[192:193], v[72:73] op_sel_hi:[1,0]
	v_pk_fma_f32 v[88:89], v[194:195], v[88:89], v[198:199]
	v_pk_fma_f32 v[76:77], v[196:197], v[76:77], v[200:201]
	s_waitcnt vmcnt(6)
	v_mov_b64_e32 v[196:197], v[252:253]
	v_mov_b64_e32 v[198:199], v[254:255]
	global_load_dwordx4 v[252:255], v[30:31], off
	s_waitcnt vmcnt(6)
	v_mov_b64_e32 v[220:221], v[224:225]
	v_mov_b64_e32 v[222:223], v[226:227]
	global_load_dwordx4 v[224:227], v[32:33], off
	v_pk_fma_f32 v[192:193], v[66:67], v[198:199], v[222:223]
	v_pk_fma_f32 v[194:195], v[64:65], v[196:197], v[220:221]
	v_pk_mul_f32 v[64:65], v[84:85], v[42:43] op_sel_hi:[1,0]
	v_pk_mul_f32 v[66:67], v[86:87], v[42:43] op_sel_hi:[1,0]
	v_pk_fma_f32 v[186:187], v[64:65], v[196:197], v[220:221]
	v_pk_fma_f32 v[134:135], v[66:67], v[198:199], v[222:223]
	v_pk_mul_f32 v[64:65], v[112:113], v[48:49] op_sel_hi:[1,0]
	v_pk_mul_f32 v[66:67], v[114:115], v[48:49] op_sel_hi:[1,0]
	v_pk_fma_f32 v[86:87], v[64:65], v[196:197], v[220:221]
	v_pk_fma_f32 v[84:85], v[66:67], v[198:199], v[222:223]
	v_pk_mul_f32 v[66:67], v[130:131], v[72:73] op_sel_hi:[1,0]
	v_pk_mul_f32 v[64:65], v[132:133], v[72:73] op_sel_hi:[1,0]
	v_pk_fma_f32 v[66:67], v[196:197], v[66:67], v[220:221]
	v_pk_fma_f32 v[64:65], v[198:199], v[64:65], v[222:223]
	s_waitcnt vmcnt(6)
	v_mov_b64_e32 v[196:197], v[228:229]
	v_mov_b64_e32 v[198:199], v[230:231]
	global_load_dwordx4 v[228:231], v[34:35], off
	s_waitcnt vmcnt(6)
	v_mov_b64_e32 v[220:221], v[232:233]
	v_mov_b64_e32 v[222:223], v[234:235]
	v_pk_fma_f32 v[114:115], v[56:57], v[198:199], v[222:223]
	v_pk_fma_f32 v[130:131], v[8:9], v[196:197], v[220:221]
	v_pk_mul_f32 v[8:9], v[74:75], v[42:43] op_sel_hi:[1,0]
	v_pk_mul_f32 v[56:57], v[70:71], v[42:43] op_sel_hi:[1,0]
	v_pk_fma_f32 v[112:113], v[8:9], v[196:197], v[220:221]
	v_pk_fma_f32 v[74:75], v[56:57], v[198:199], v[222:223]
	v_pk_mul_f32 v[8:9], v[110:111], v[48:49] op_sel_hi:[1,0]
	v_pk_mul_f32 v[56:57], v[106:107], v[48:49] op_sel_hi:[1,0]
	v_pk_fma_f32 v[68:69], v[8:9], v[196:197], v[220:221]
	v_pk_fma_f32 v[60:61], v[56:57], v[198:199], v[222:223]
	v_pk_mul_f32 v[8:9], v[128:129], v[72:73] op_sel_hi:[1,0]
	v_pk_mul_f32 v[56:57], v[124:125], v[72:73] op_sel_hi:[1,0]
	v_pk_fma_f32 v[58:59], v[196:197], v[8:9], v[220:221]
	v_pk_fma_f32 v[56:57], v[198:199], v[56:57], v[222:223]
	s_waitcnt vmcnt(5)
	v_mov_b64_e32 v[196:197], v[236:237]
	v_mov_b64_e32 v[198:199], v[238:239]
	s_waitcnt vmcnt(4)
	v_mov_b64_e32 v[220:221], v[244:245]
	v_mov_b64_e32 v[222:223], v[246:247]
	v_pk_mul_f32 v[8:9], v[140:141], v[10:11] op_sel_hi:[1,0]
	v_max_f32_e64 v10, |v84|, |v85|
	v_max3_f32 v10, |v86|, |v87|, v10
	v_pk_fma_f32 v[124:125], v[8:9], v[198:199], v[222:223]
	v_pk_fma_f32 v[126:127], v[6:7], v[196:197], v[220:221]
	v_pk_mul_f32 v[6:7], v[62:63], v[42:43] op_sel_hi:[1,0]
	v_pk_mul_f32 v[8:9], v[150:151], v[42:43] op_sel_hi:[1,0]
	v_pk_fma_f32 v[108:109], v[6:7], v[196:197], v[220:221]
	v_pk_fma_f32 v[106:107], v[8:9], v[198:199], v[222:223]
	v_pk_mul_f32 v[6:7], v[102:103], v[48:49] op_sel_hi:[1,0]
	v_pk_mul_f32 v[8:9], v[160:161], v[48:49] op_sel_hi:[1,0]
	v_pk_fma_f32 v[102:103], v[6:7], v[196:197], v[220:221]
	v_pk_fma_f32 v[90:91], v[8:9], v[198:199], v[222:223]
	v_pk_mul_f32 v[6:7], v[122:123], v[72:73] op_sel_hi:[1,0]
	v_pk_mul_f32 v[8:9], v[178:179], v[72:73] op_sel_hi:[1,0]
	v_pk_fma_f32 v[70:71], v[6:7], v[196:197], v[220:221]
	v_pk_fma_f32 v[62:63], v[8:9], v[198:199], v[222:223]
	s_waitcnt vmcnt(3)
; template <bool WB = true>
; __device__ __forceinline__ void ln1_phase(const bf16_t* buf, bf16_t* h1b, unsigned* xqs, float* sx, const float* gam, const float* bet, int G, int b) {
;     ...
;         for (int q = 0; q < R; ++q) { amax[q] = 0.f;
; #pragma unroll
;             for (int j = 0; j < 8; ++j) amax[q] = fmaxf(amax[q], fmaxf(fmaxf(fabsf(v[q][j].x), fabsf(v[q][j].y)), fmaxf(fabsf(v[q][j].z), fabsf(v[q][j].w)))); }
; #pragma unroll
;         for (int q = 0; q < R; ++q) amax[q] = wave_max(amax[q]);
; #pragma unroll
;         for (int q = 0; q < R; ++q) {
;             const int row = row0 + q * NGW;
;             if (row < S_) {
;                 const float inv = amax[q] > 0.f ? 127.0f / amax[q] : 0.f;
;                 if (lane == 0) sx[row] = amax[q] * (1.0f / 127.0f);
	v_mov_b64_e32 v[6:7], v[248:249]
	v_mov_b64_e32 v[8:9], v[250:251]
	s_waitcnt vmcnt(2)
	v_mov_b64_e32 v[196:197], v[252:253]
	v_mov_b64_e32 v[198:199], v[254:255]
	v_pk_fma_f32 v[122:123], v[4:5], v[8:9], v[198:199]
	v_pk_fma_f32 v[128:129], v[2:3], v[6:7], v[196:197]
	v_pk_mul_f32 v[2:3], v[52:53], v[42:43] op_sel_hi:[1,0]
	v_pk_mul_f32 v[4:5], v[54:55], v[42:43] op_sel_hi:[1,0]
	v_pk_fma_f32 v[120:121], v[2:3], v[6:7], v[196:197]
	v_pk_fma_f32 v[110:111], v[4:5], v[8:9], v[198:199]
	v_pk_mul_f32 v[2:3], v[92:93], v[48:49] op_sel_hi:[1,0]
	v_pk_mul_f32 v[4:5], v[94:95], v[48:49] op_sel_hi:[1,0]
	v_pk_fma_f32 v[94:95], v[2:3], v[6:7], v[196:197]
	v_pk_fma_f32 v[92:93], v[4:5], v[8:9], v[198:199]
	v_pk_mul_f32 v[2:3], v[116:117], v[72:73] op_sel_hi:[1,0]
	v_pk_mul_f32 v[4:5], v[118:119], v[72:73] op_sel_hi:[1,0]
	v_pk_fma_f32 v[54:55], v[2:3], v[6:7], v[196:197]
	v_pk_fma_f32 v[52:53], v[4:5], v[8:9], v[198:199]
	s_waitcnt vmcnt(1)
	v_mov_b64_e32 v[2:3], v[224:225]
	v_mov_b64_e32 v[4:5], v[226:227]
	s_waitcnt vmcnt(0)
	v_mov_b64_e32 v[6:7], v[228:229]
	v_mov_b64_e32 v[8:9], v[230:231]
	v_pk_fma_f32 v[116:117], v[40:41], v[4:5], v[8:9]
	v_pk_mul_f32 v[40:41], v[50:51], v[42:43] op_sel_hi:[1,0]
	v_pk_mul_f32 v[42:43], v[46:47], v[42:43] op_sel_hi:[1,0]
	v_pk_fma_f32 v[118:119], v[44:45], v[2:3], v[6:7]
	v_pk_fma_f32 v[44:45], v[42:43], v[4:5], v[8:9]
	v_pk_fma_f32 v[46:47], v[40:41], v[2:3], v[6:7]
	v_pk_mul_f32 v[42:43], v[82:83], v[48:49] op_sel_hi:[1,0]
	v_pk_mul_f32 v[40:41], v[78:79], v[48:49] op_sel_hi:[1,0]
	v_pk_mul_f32 v[48:49], v[100:101], v[72:73] op_sel_hi:[1,0]
	v_pk_fma_f32 v[42:43], v[42:43], v[2:3], v[6:7]
	v_pk_fma_f32 v[2:3], v[48:49], v[2:3], v[6:7]
	v_max_f32_e64 v6, |v172|, |v173|
	v_max_f32_e64 v7, |v182|, |v183|
	v_pk_mul_f32 v[50:51], v[96:97], v[72:73] op_sel_hi:[1,0]
	v_max3_f32 v6, |v174|, |v175|, v6
	v_max3_f32 v7, |v184|, |v185|, v7
	v_pk_fma_f32 v[40:41], v[40:41], v[4:5], v[8:9]
	v_pk_fma_f32 v[4:5], v[50:51], v[4:5], v[8:9]
	v_max3_f32 v6, v6, 0, v7
	v_max_f32_e64 v7, |v188|, |v189|
	v_max_f32_e64 v8, |v192|, |v193|
	v_max3_f32 v7, |v190|, |v191|, v7
	v_max3_f32 v8, |v194|, |v195|, v8
	v_max3_f32 v6, v6, v7, v8
	v_max_f32_e64 v7, |v114|, |v115|
	v_max_f32_e64 v8, |v124|, |v125|
	v_max3_f32 v7, |v130|, |v131|, v7
	v_max3_f32 v8, |v126|, |v127|, v8
	v_max3_f32 v6, v6, v7, v8
	v_max_f32_e64 v7, |v122|, |v123|
	v_max_f32_e64 v8, |v116|, |v117|
	v_max3_f32 v7, |v128|, |v129|, v7
	v_max3_f32 v8, |v118|, |v119|, v8
	v_max3_f32 v6, v6, v7, v8
	v_max_f32_e64 v7, |v152|, |v153|
	v_max_f32_e64 v8, |v164|, |v165|
	v_max3_f32 v7, |v154|, |v155|, v7
	v_max3_f32 v8, |v170|, |v171|, v8
	v_max3_f32 v7, v7, 0, v8
	v_max_f32_e64 v8, |v176|, |v177|
	v_max_f32_e64 v9, |v134|, |v135|
	v_max3_f32 v8, |v180|, |v181|, v8
	v_max3_f32 v9, |v186|, |v187|, v9
	v_max3_f32 v7, v7, v8, v9
	v_max_f32_e64 v8, |v74|, |v75|
	v_max_f32_e64 v9, |v106|, |v107|
	v_max3_f32 v8, |v112|, |v113|, v8
	v_max3_f32 v9, |v108|, |v109|, v9
	v_max3_f32 v7, v7, v8, v9
	v_max_f32_e64 v8, |v110|, |v111|
	v_max_f32_e64 v9, |v44|, |v45|
	v_max3_f32 v8, |v120|, |v121|, v8
	v_max3_f32 v9, |v46|, |v47|, v9
	v_max3_f32 v7, v7, v8, v9
	v_max_f32_e64 v8, |v142|, |v143|
	v_max_f32_e64 v9, |v156|, |v157|
	v_max3_f32 v8, |v144|, |v145|, v8
	v_max3_f32 v9, |v158|, |v159|, v9
	v_max3_f32 v8, v8, 0, v9
	v_max_f32_e64 v9, |v104|, |v105|
	v_max3_f32 v9, |v162|, |v163|, v9
	v_max3_f32 v8, v8, v9, v10
	v_max_f32_e64 v9, |v60|, |v61|
	v_max_f32_e64 v10, |v90|, |v91|
	v_max3_f32 v9, |v68|, |v69|, v9
	v_max3_f32 v10, |v102|, |v103|, v10
	v_max3_f32 v8, v8, v9, v10
	v_max_f32_e64 v9, |v92|, |v93|
	v_max_f32_e64 v10, |v40|, |v41|
	v_max3_f32 v9, |v94|, |v95|, v9
	v_max3_f32 v10, |v42|, |v43|, v10
	v_max3_f32 v8, v8, v9, v10
	v_max_f32_e64 v9, |v136|, |v137|
	v_max_f32_e64 v10, |v146|, |v147|
	v_max3_f32 v9, |v138|, |v139|, v9
	v_max3_f32 v10, |v148|, |v149|, v10
	v_max3_f32 v9, v9, 0, v10
	v_max_f32_e64 v10, |v76|, |v77|
	v_max_f32_e64 v48, |v64|, |v65|
	v_max3_f32 v10, |v88|, |v89|, v10
	v_max3_f32 v48, |v66|, |v67|, v48
	v_max3_f32 v9, v9, v10, v48
	v_max_f32_e64 v10, |v56|, |v57|
	v_max_f32_e64 v48, |v62|, |v63|
	v_max3_f32 v10, |v58|, |v59|, v10
	v_max3_f32 v48, |v70|, |v71|, v48
	v_max3_f32 v9, v9, v10, v48
	v_max_f32_e64 v10, |v52|, |v53|
	v_max_f32_e64 v48, |v4|, |v5|
	v_max3_f32 v10, |v54|, |v55|, v10
	v_max3_f32 v48, |v2|, |v3|, v48
	v_max3_f32 v9, v9, v10, v48
	ds_bpermute_b32 v10, v167, v6
	s_waitcnt lgkmcnt(0)
	v_max_f32_e32 v10, v10, v10
	v_max_f32_e32 v6, v6, v10
	ds_bpermute_b32 v10, v169, v6
	s_waitcnt lgkmcnt(0)
	v_max_f32_e32 v10, v10, v10
	v_max_f32_e32 v6, v6, v10
	ds_bpermute_b32 v10, v213, v6
	s_waitcnt lgkmcnt(0)
	v_max_f32_e32 v10, v10, v10
	v_max_f32_e32 v6, v6, v10
	ds_bpermute_b32 v10, v214, v6
	s_waitcnt lgkmcnt(0)
	v_max_f32_e32 v10, v10, v10
	v_max_f32_e32 v6, v6, v10
	ds_bpermute_b32 v10, v215, v6
	s_waitcnt lgkmcnt(0)
	v_max_f32_e32 v10, v10, v10
	v_max_f32_e32 v6, v6, v10
	ds_bpermute_b32 v10, v216, v6
	s_waitcnt lgkmcnt(0)
	v_max_f32_e32 v10, v10, v10
	v_max_f32_e32 v10, v6, v10
	ds_bpermute_b32 v6, v167, v7
	s_waitcnt lgkmcnt(0)
	v_max_f32_e32 v6, v6, v6
	v_max_f32_e32 v6, v7, v6
	ds_bpermute_b32 v7, v169, v6
	s_waitcnt lgkmcnt(0)
	v_max_f32_e32 v7, v7, v7
	v_max_f32_e32 v6, v6, v7
	ds_bpermute_b32 v7, v213, v6
	s_waitcnt lgkmcnt(0)
	v_max_f32_e32 v7, v7, v7
	v_max_f32_e32 v6, v6, v7
	ds_bpermute_b32 v7, v214, v6
	s_waitcnt lgkmcnt(0)
	v_max_f32_e32 v7, v7, v7
	v_max_f32_e32 v6, v6, v7
	ds_bpermute_b32 v7, v215, v6
	s_waitcnt lgkmcnt(0)
	v_max_f32_e32 v7, v7, v7
	v_max_f32_e32 v48, v6, v7
	ds_bpermute_b32 v6, v167, v8
	ds_bpermute_b32 v49, v216, v48
	s_waitcnt lgkmcnt(1)
	v_max_f32_e32 v6, v6, v6
	v_max_f32_e32 v6, v8, v6
	ds_bpermute_b32 v8, v167, v9
	ds_bpermute_b32 v7, v169, v6
	s_waitcnt lgkmcnt(1)
	v_max_f32_e32 v8, v8, v8
	v_max_f32_e32 v8, v9, v8
	ds_bpermute_b32 v9, v169, v8
	s_waitcnt lgkmcnt(1)
	v_max_f32_e32 v7, v7, v7
	v_max_f32_e32 v6, v6, v7
	ds_bpermute_b32 v7, v213, v6
	s_waitcnt lgkmcnt(1)
	v_max_f32_e32 v9, v9, v9
	v_max_f32_e32 v8, v8, v9
	ds_bpermute_b32 v9, v213, v8
	s_waitcnt lgkmcnt(1)
	v_max_f32_e32 v7, v7, v7
	v_max_f32_e32 v6, v6, v7
	ds_bpermute_b32 v7, v214, v6
	s_waitcnt lgkmcnt(1)
	v_max_f32_e32 v9, v9, v9
	v_max_f32_e32 v8, v8, v9
	ds_bpermute_b32 v9, v214, v8
	s_waitcnt lgkmcnt(1)
	v_max_f32_e32 v7, v7, v7
	v_max_f32_e32 v6, v6, v7
	ds_bpermute_b32 v7, v215, v6
	s_waitcnt lgkmcnt(1)
	v_max_f32_e32 v9, v9, v9
	v_max_f32_e32 v8, v8, v9
	ds_bpermute_b32 v9, v215, v8
	s_waitcnt lgkmcnt(1)
	v_max_f32_e32 v7, v7, v7
	v_max_f32_e32 v6, v6, v7
	ds_bpermute_b32 v7, v216, v6
	s_waitcnt lgkmcnt(1)
	v_max_f32_e32 v9, v9, v9
	v_max_f32_e32 v8, v8, v9
	ds_bpermute_b32 v9, v216, v8
	s_and_saveexec_b64 s[0:1], s[38:39]
	s_cbranch_execz .LBB0_545
	s_add_u32 s8, s92, s6
	v_mul_f32_e32 v50, 0x3c010204, v10
	s_addc_u32 s9, s93, s7
	global_store_dword v11, v50, s[8:9]
